# v24
# baseline (speedup 1.0000x reference)
.LBB1_12:
	s_waitcnt vmcnt(8)
	s_waitcnt lgkmcnt(0)
	s_barrier
	v_mfma_f32_16x16x32_f16 v[128:131], v[148:151], v[166:169], v[128:131]
	v_mfma_f32_16x16x32_f16 v[128:131], v[152:155], v[174:177], v[128:131]
	v_mfma_f32_16x16x32_f16 v[120:123], v[160:163], v[174:177], v[120:123]
	v_mfma_f32_16x16x32_f16 v[120:123], v[156:159], v[166:169], v[120:123]
	v_mfma_f32_16x16x32_f16 v[104:107], v[156:159], v[170:173], v[104:107]
	v_mfma_f32_16x16x32_f16 v[104:107], v[160:163], v[178:181], v[104:107]
	v_mfma_f32_16x16x32_f16 v[112:115], v[152:155], v[178:181], v[112:115]
	v_mfma_f32_16x16x32_f16 v[112:115], v[148:151], v[170:173], v[112:115]
	v_mfma_f32_16x16x32_f16 v[96:99], v[148:151], v[182:185], v[96:99]
	v_mfma_f32_16x16x32_f16 v[96:99], v[152:155], v[190:193], v[96:99]
	v_mfma_f32_16x16x32_f16 v[88:91], v[160:163], v[190:193], v[88:91]
	v_mfma_f32_16x16x32_f16 v[88:91], v[156:159], v[182:185], v[88:91]
	v_mfma_f32_16x16x32_f16 v[72:75], v[156:159], v[186:189], v[72:75]
	v_mfma_f32_16x16x32_f16 v[72:75], v[160:163], v[214:217], v[72:75]
	v_mfma_f32_16x16x32_f16 v[80:83], v[152:155], v[214:217], v[80:83]
	v_mfma_f32_16x16x32_f16 v[80:83], v[148:151], v[186:189], v[80:83]
	v_mfma_f32_16x16x32_f16 v[124:127], v[132:135], v[166:169], v[124:127]
	v_mfma_f32_16x16x32_f16 v[124:127], v[136:139], v[174:177], v[124:127]
	v_mfma_f32_16x16x32_f16 v[116:119], v[144:147], v[174:177], v[116:119]
	v_mfma_f32_16x16x32_f16 v[116:119], v[140:143], v[166:169], v[116:119]
	v_mfma_f32_16x16x32_f16 v[100:103], v[140:143], v[170:173], v[100:103]
	v_mfma_f32_16x16x32_f16 v[100:103], v[144:147], v[178:181], v[100:103]
	v_mfma_f32_16x16x32_f16 v[108:111], v[136:139], v[178:181], v[108:111]
	v_mfma_f32_16x16x32_f16 v[108:111], v[132:135], v[170:173], v[108:111]
	v_mfma_f32_16x16x32_f16 v[92:95], v[132:135], v[182:185], v[92:95]
	v_mfma_f32_16x16x32_f16 v[92:95], v[136:139], v[190:193], v[92:95]
	v_mfma_f32_16x16x32_f16 v[84:87], v[144:147], v[190:193], v[84:87]
	v_mfma_f32_16x16x32_f16 v[84:87], v[140:143], v[182:185], v[84:87]
	v_mfma_f32_16x16x32_f16 v[68:71], v[140:143], v[186:189], v[68:71]
	v_mfma_f32_16x16x32_f16 v[68:71], v[144:147], v[214:217], v[68:71]
	v_mfma_f32_16x16x32_f16 v[76:79], v[136:139], v[214:217], v[76:79]
	v_mfma_f32_16x16x32_f16 v[76:79], v[132:135], v[186:189], v[76:79]
	s_barrier
	s_andn2_b64 vcc, exec, s[4:5]
	s_cbranch_vccnz .LBB1_16
	v_cvt_pkrtz_f16_f32 v166, v0, v1
	v_cvt_pkrtz_f16_f32 v167, v2, v3
	v_add_u32_e32 v166, 0x20002, v166
	v_add_u32_e32 v167, 0x20002, v167
	v_and_b32_e32 v166, 0xfffcfffc, v166
	v_and_b32_e32 v167, 0xfffcfffc, v167
	global_store_dwordx2 v231, v[166:167], s[90:91]

.LBB1_20:
	s_waitcnt lgkmcnt(0)
	s_barrier
	v_mfma_f32_16x16x32_f16 v[64:67], v[148:151], v[188:191], v[64:67]
	v_mfma_f32_16x16x32_f16 v[64:67], v[152:155], v[192:195], v[64:67]
	v_mfma_f32_16x16x32_f16 v[56:59], v[160:163], v[192:195], v[56:59]
	v_mfma_f32_16x16x32_f16 v[56:59], v[156:159], v[188:191], v[56:59]
	v_mfma_f32_16x16x32_f16 v[40:43], v[156:159], v[176:179], v[40:43]
	v_mfma_f32_16x16x32_f16 v[40:43], v[160:163], v[180:183], v[40:43]
	v_mfma_f32_16x16x32_f16 v[48:51], v[152:155], v[180:183], v[48:51]
	v_mfma_f32_16x16x32_f16 v[48:51], v[148:151], v[176:179], v[48:51]
	v_mfma_f32_16x16x32_f16 v[32:35], v[148:151], v[172:175], v[32:35]
	v_mfma_f32_16x16x32_f16 v[32:35], v[152:155], v[184:187], v[32:35]
	v_mfma_f32_16x16x32_f16 v[24:27], v[160:163], v[184:187], v[24:27]
	v_mfma_f32_16x16x32_f16 v[24:27], v[156:159], v[172:175], v[24:27]
	v_mfma_f32_16x16x32_f16 v[8:11], v[156:159], v[164:167], v[8:11]
	v_mfma_f32_16x16x32_f16 v[8:11], v[160:163], v[168:171], v[8:11]
	v_mfma_f32_16x16x32_f16 v[16:19], v[152:155], v[168:171], v[16:19]
	v_mfma_f32_16x16x32_f16 v[16:19], v[148:151], v[164:167], v[16:19]
	v_mfma_f32_16x16x32_f16 v[60:63], v[132:135], v[188:191], v[60:63]
	v_mfma_f32_16x16x32_f16 v[60:63], v[136:139], v[192:195], v[60:63]
	v_mfma_f32_16x16x32_f16 v[52:55], v[144:147], v[192:195], v[52:55]
	v_mfma_f32_16x16x32_f16 v[52:55], v[140:143], v[188:191], v[52:55]
	v_mfma_f32_16x16x32_f16 v[36:39], v[140:143], v[176:179], v[36:39]
	v_mfma_f32_16x16x32_f16 v[36:39], v[144:147], v[180:183], v[36:39]
	v_mfma_f32_16x16x32_f16 v[44:47], v[136:139], v[180:183], v[44:47]
	v_mfma_f32_16x16x32_f16 v[44:47], v[132:135], v[176:179], v[44:47]
	v_mfma_f32_16x16x32_f16 v[28:31], v[132:135], v[172:175], v[28:31]
	v_mfma_f32_16x16x32_f16 v[28:31], v[136:139], v[184:187], v[28:31]
	v_mfma_f32_16x16x32_f16 v[20:23], v[144:147], v[184:187], v[20:23]
	v_mfma_f32_16x16x32_f16 v[20:23], v[140:143], v[172:175], v[20:23]
	v_mfma_f32_16x16x32_f16 v[4:7], v[140:143], v[164:167], v[4:7]
	v_mfma_f32_16x16x32_f16 v[4:7], v[144:147], v[168:171], v[4:7]
	v_mfma_f32_16x16x32_f16 v[12:15], v[136:139], v[168:171], v[12:15]
	v_mfma_f32_16x16x32_f16 v[12:15], v[132:135], v[164:167], v[12:15]
	s_barrier
	s_add_u32 s48, s48, 0x100000
	ds_read_b128 v[148:151], v228 offset:32768
	ds_read_b128 v[152:155], v229 offset:32768
	s_addc_u32 s49, s49, 0
	s_mov_b32 m0, s57
	ds_read_b128 v[156:159], v228 offset:34816
	ds_read_b128 v[160:163], v229 offset:34816
	ds_read_b128 v[132:135], v228 offset:49152
	ds_read_b128 v[136:139], v229 offset:49152
	ds_read_b128 v[140:143], v228 offset:51200
	ds_read_b128 v[144:147], v229 offset:51200
	ds_read_b128 v[188:191], v226 offset:32768
	ds_read_b128 v[176:179], v226 offset:34816
	ds_read_b128 v[192:195], v227 offset:32768
	ds_read_b128 v[180:183], v227 offset:34816
	ds_read_b128 v[172:175], v226 offset:36864
	ds_read_b128 v[164:167], v226 offset:38912
	ds_read_b128 v[184:187], v227 offset:36864
	ds_read_b128 v[168:171], v227 offset:38912
	global_load_lds_dwordx4 v202, s[48:49]
	s_mov_b32 m0, s58
	s_nop 0
	global_load_lds_dwordx4 v198, s[48:49]
	s_mov_b64 s[48:49], -1
	s_mov_b64 vcc, s[4:5]
	s_cbranch_vccz .LBB1_22
	s_waitcnt vmcnt(8)
	s_mov_b64 s[48:49], 0

.LBB1_24:
	s_waitcnt lgkmcnt(0)
	s_barrier
	v_mfma_f32_16x16x32_f16 v[128:131], v[148:151], v[188:191], v[128:131]
	v_mfma_f32_16x16x32_f16 v[128:131], v[152:155], v[192:195], v[128:131]
	v_mfma_f32_16x16x32_f16 v[120:123], v[160:163], v[192:195], v[120:123]
	v_mfma_f32_16x16x32_f16 v[120:123], v[156:159], v[188:191], v[120:123]
	v_mfma_f32_16x16x32_f16 v[104:107], v[156:159], v[176:179], v[104:107]
	v_mfma_f32_16x16x32_f16 v[104:107], v[160:163], v[180:183], v[104:107]
	v_mfma_f32_16x16x32_f16 v[112:115], v[152:155], v[180:183], v[112:115]
	v_mfma_f32_16x16x32_f16 v[112:115], v[148:151], v[176:179], v[112:115]
	v_mfma_f32_16x16x32_f16 v[96:99], v[148:151], v[172:175], v[96:99]
	v_mfma_f32_16x16x32_f16 v[96:99], v[152:155], v[184:187], v[96:99]
	v_mfma_f32_16x16x32_f16 v[88:91], v[160:163], v[184:187], v[88:91]
	v_mfma_f32_16x16x32_f16 v[88:91], v[156:159], v[172:175], v[88:91]
	v_mfma_f32_16x16x32_f16 v[72:75], v[156:159], v[164:167], v[72:75]
	v_mfma_f32_16x16x32_f16 v[72:75], v[160:163], v[168:171], v[72:75]
	v_mfma_f32_16x16x32_f16 v[80:83], v[152:155], v[168:171], v[80:83]
	v_mfma_f32_16x16x32_f16 v[80:83], v[148:151], v[164:167], v[80:83]
	v_mfma_f32_16x16x32_f16 v[124:127], v[132:135], v[188:191], v[124:127]
	v_mfma_f32_16x16x32_f16 v[124:127], v[136:139], v[192:195], v[124:127]
	v_mfma_f32_16x16x32_f16 v[116:119], v[144:147], v[192:195], v[116:119]
	v_mfma_f32_16x16x32_f16 v[116:119], v[140:143], v[188:191], v[116:119]
	v_mfma_f32_16x16x32_f16 v[100:103], v[140:143], v[176:179], v[100:103]
	v_mfma_f32_16x16x32_f16 v[100:103], v[144:147], v[180:183], v[100:103]
	v_mfma_f32_16x16x32_f16 v[108:111], v[136:139], v[180:183], v[108:111]
	v_mfma_f32_16x16x32_f16 v[108:111], v[132:135], v[176:179], v[108:111]
	v_mfma_f32_16x16x32_f16 v[92:95], v[132:135], v[172:175], v[92:95]
	v_mfma_f32_16x16x32_f16 v[92:95], v[136:139], v[184:187], v[92:95]
	v_mfma_f32_16x16x32_f16 v[84:87], v[144:147], v[184:187], v[84:87]
	v_mfma_f32_16x16x32_f16 v[84:87], v[140:143], v[172:175], v[84:87]
	v_mfma_f32_16x16x32_f16 v[68:71], v[140:143], v[164:167], v[68:71]
	v_mfma_f32_16x16x32_f16 v[68:71], v[144:147], v[168:171], v[68:71]
	v_mfma_f32_16x16x32_f16 v[76:79], v[136:139], v[168:171], v[76:79]
	v_mfma_f32_16x16x32_f16 v[76:79], v[132:135], v[164:167], v[76:79]
	s_barrier
	s_mov_b32 m0, s59
	s_add_u32 s4, s46, 0x100080
	ds_read_b128 v[164:167], v226 offset:49152
	ds_read_b128 v[168:171], v226 offset:51200
	ds_read_b128 v[172:175], v227 offset:49152
	ds_read_b128 v[176:179], v227 offset:51200
	ds_read_b128 v[180:183], v226 offset:53248
	ds_read_b128 v[184:187], v226 offset:55296
	ds_read_b128 v[188:191], v227 offset:53248
	ds_read_b128 v[192:195], v227 offset:55296
	global_load_lds_dwordx4 v200, s[84:85]
	s_mov_b32 m0, s60
	s_addc_u32 s5, s47, 0
	global_load_lds_dwordx4 v196, s[84:85]
	s_mov_b32 m0, s63
	s_nop 0
	global_load_lds_dwordx4 v200, s[4:5]
	s_mov_b32 m0, s64
	s_nop 0
	global_load_lds_dwordx4 v196, s[4:5]
	s_mov_b32 m0, s61
	s_nop 0
	global_load_lds_dwordx4 v202, s[86:87]
	s_mov_b32 m0, s62
	s_nop 0
	global_load_lds_dwordx4 v198, s[86:87]
	s_waitcnt vmcnt(8)
	s_waitcnt lgkmcnt(0)
	s_barrier
	v_mfma_f32_16x16x32_f16 v[64:67], v[148:151], v[164:167], v[64:67]
	v_mfma_f32_16x16x32_f16 v[64:67], v[152:155], v[172:175], v[64:67]
	v_mfma_f32_16x16x32_f16 v[56:59], v[160:163], v[172:175], v[56:59]
	v_mfma_f32_16x16x32_f16 v[56:59], v[156:159], v[164:167], v[56:59]
	v_mfma_f32_16x16x32_f16 v[40:43], v[156:159], v[168:171], v[40:43]
	v_mfma_f32_16x16x32_f16 v[40:43], v[160:163], v[176:179], v[40:43]
	v_mfma_f32_16x16x32_f16 v[48:51], v[152:155], v[176:179], v[48:51]
	v_mfma_f32_16x16x32_f16 v[48:51], v[148:151], v[168:171], v[48:51]
	v_mfma_f32_16x16x32_f16 v[32:35], v[148:151], v[180:183], v[32:35]
	v_mfma_f32_16x16x32_f16 v[32:35], v[152:155], v[188:191], v[32:35]
	v_mfma_f32_16x16x32_f16 v[24:27], v[160:163], v[188:191], v[24:27]
	v_mfma_f32_16x16x32_f16 v[24:27], v[156:159], v[180:183], v[24:27]
	v_mfma_f32_16x16x32_f16 v[8:11], v[156:159], v[184:187], v[8:11]
	v_mfma_f32_16x16x32_f16 v[8:11], v[160:163], v[192:195], v[8:11]
	v_mfma_f32_16x16x32_f16 v[16:19], v[152:155], v[192:195], v[16:19]
	v_mfma_f32_16x16x32_f16 v[16:19], v[148:151], v[184:187], v[16:19]
	v_mfma_f32_16x16x32_f16 v[60:63], v[132:135], v[164:167], v[60:63]
	v_mfma_f32_16x16x32_f16 v[60:63], v[136:139], v[172:175], v[60:63]
	v_mfma_f32_16x16x32_f16 v[52:55], v[144:147], v[172:175], v[52:55]
	v_mfma_f32_16x16x32_f16 v[52:55], v[140:143], v[164:167], v[52:55]
	v_mfma_f32_16x16x32_f16 v[36:39], v[140:143], v[168:171], v[36:39]
	v_mfma_f32_16x16x32_f16 v[36:39], v[144:147], v[176:179], v[36:39]
	v_mfma_f32_16x16x32_f16 v[44:47], v[136:139], v[176:179], v[44:47]
	v_mfma_f32_16x16x32_f16 v[44:47], v[132:135], v[168:171], v[44:47]
	v_mfma_f32_16x16x32_f16 v[28:31], v[132:135], v[180:183], v[28:31]
	v_mfma_f32_16x16x32_f16 v[28:31], v[136:139], v[188:191], v[28:31]
	v_mfma_f32_16x16x32_f16 v[20:23], v[144:147], v[188:191], v[20:23]
	v_mfma_f32_16x16x32_f16 v[20:23], v[140:143], v[180:183], v[20:23]
	v_mfma_f32_16x16x32_f16 v[4:7], v[140:143], v[184:187], v[4:7]
	v_mfma_f32_16x16x32_f16 v[4:7], v[144:147], v[192:195], v[4:7]
	v_mfma_f32_16x16x32_f16 v[12:15], v[136:139], v[192:195], v[12:15]
	v_mfma_f32_16x16x32_f16 v[12:15], v[132:135], v[184:187], v[12:15]
	s_barrier
	s_add_u32 s80, s80, 0x100
	s_addc_u32 s81, s81, 0
	s_add_u32 s44, s44, 0x100
	s_addc_u32 s45, s45, 0
	s_cmp_gt_u32 s82, 61
	s_cbranch_scc1 .LBB1_4
	s_mov_b32 s48, s82
	s_branch .LBB1_9

.LBB1_30:
	s_endpgm
	s_nop 0
	s_nop 0
	s_nop 0
	s_endpgm

.LBB2_20:
	s_add_u32 s30, s28, 0xffc80080
	s_addc_u32 s31, s29, -1
	s_cmpk_eq_i32 s58, 0xdc
	s_cselect_b32 s35, s25, s31
	s_cselect_b32 s34, s24, s30
	s_cselect_b32 s31, s27, s57
	s_cselect_b32 s30, s26, s56
	s_add_i32 m0, s37, 0xc000
	ds_read_b128 v[166:169], v143
	ds_read_b128 v[170:173], v147
	ds_read_b128 v[174:177], v149
	ds_read_b128 v[178:181], v150
	ds_read_b128 v[182:185], v151
	ds_read_b128 v[186:189], v152
	ds_read_b128 v[190:193], v153
	ds_read_b128 v[194:197], v154
	ds_read_b128 v[198:201], v155
	ds_read_b128 v[202:205], v155 offset:2048
	ds_read_b128 v[206:209], v156
	ds_read_b128 v[210:213], v156 offset:2048
	ds_read_b128 v[214:217], v155 offset:4096
	ds_read_b128 v[218:221], v155 offset:6144
	ds_read_b128 v[222:225], v156 offset:4096
	ds_read_b128 v[226:229], v156 offset:6144
	global_load_lds_dwordx4 v134, s[28:29]
	s_add_i32 m0, s37, 0xe000
	s_nop 0
	global_load_lds_dwordx4 v132, s[28:29]
	s_waitcnt vmcnt(8)
	s_waitcnt lgkmcnt(0)
	s_barrier
	v_mfma_f32_16x16x32_f16 v[124:127], v[166:169], v[198:201], v[124:127]
	v_mfma_f32_16x16x32_f16 v[124:127], v[170:173], v[206:209], v[124:127]
	v_mfma_f32_16x16x32_f16 v[120:123], v[178:181], v[206:209], v[120:123]
	v_mfma_f32_16x16x32_f16 v[120:123], v[174:177], v[198:201], v[120:123]
	v_mfma_f32_16x16x32_f16 v[112:115], v[174:177], v[202:205], v[112:115]
	v_mfma_f32_16x16x32_f16 v[112:115], v[178:181], v[210:213], v[112:115]
	v_mfma_f32_16x16x32_f16 v[116:119], v[170:173], v[210:213], v[116:119]
	v_mfma_f32_16x16x32_f16 v[116:119], v[166:169], v[202:205], v[116:119]
	v_mfma_f32_16x16x32_f16 v[108:111], v[166:169], v[214:217], v[108:111]
	v_mfma_f32_16x16x32_f16 v[108:111], v[170:173], v[222:225], v[108:111]
	v_mfma_f32_16x16x32_f16 v[100:103], v[178:181], v[222:225], v[100:103]
	v_mfma_f32_16x16x32_f16 v[100:103], v[174:177], v[214:217], v[100:103]
	v_mfma_f32_16x16x32_f16 v[84:87], v[174:177], v[218:221], v[84:87]
	v_mfma_f32_16x16x32_f16 v[84:87], v[178:181], v[226:229], v[84:87]
	v_mfma_f32_16x16x32_f16 v[92:95], v[170:173], v[226:229], v[92:95]
	v_mfma_f32_16x16x32_f16 v[92:95], v[166:169], v[218:221], v[92:95]
	v_mfma_f32_16x16x32_f16 v[104:107], v[182:185], v[198:201], v[104:107]
	v_mfma_f32_16x16x32_f16 v[104:107], v[186:189], v[206:209], v[104:107]
	v_mfma_f32_16x16x32_f16 v[96:99], v[194:197], v[206:209], v[96:99]
	v_mfma_f32_16x16x32_f16 v[96:99], v[190:193], v[198:201], v[96:99]
	v_mfma_f32_16x16x32_f16 v[80:83], v[190:193], v[202:205], v[80:83]
	v_mfma_f32_16x16x32_f16 v[80:83], v[194:197], v[210:213], v[80:83]
	v_mfma_f32_16x16x32_f16 v[88:91], v[186:189], v[210:213], v[88:91]
	v_mfma_f32_16x16x32_f16 v[88:91], v[182:185], v[202:205], v[88:91]
	v_mfma_f32_16x16x32_f16 v[76:79], v[182:185], v[214:217], v[76:79]
	v_mfma_f32_16x16x32_f16 v[76:79], v[186:189], v[222:225], v[76:79]
	v_mfma_f32_16x16x32_f16 v[72:75], v[194:197], v[222:225], v[72:75]
	v_mfma_f32_16x16x32_f16 v[72:75], v[190:193], v[214:217], v[72:75]
	v_mfma_f32_16x16x32_f16 v[64:67], v[190:193], v[218:221], v[64:67]
	v_mfma_f32_16x16x32_f16 v[64:67], v[194:197], v[226:229], v[64:67]
	v_mfma_f32_16x16x32_f16 v[68:71], v[186:189], v[226:229], v[68:71]
	v_mfma_f32_16x16x32_f16 v[68:71], v[182:185], v[218:221], v[68:71]
	s_barrier
	s_add_i32 s59, s43, s36
	s_mov_b32 m0, s59
	ds_read_b128 v[198:201], v155 offset:16384
	ds_read_b128 v[202:205], v155 offset:18432
	ds_read_b128 v[206:209], v156 offset:16384
	ds_read_b128 v[210:213], v156 offset:18432
	ds_read_b128 v[214:217], v155 offset:20480
	ds_read_b128 v[218:221], v155 offset:22528
	ds_read_b128 v[222:225], v156 offset:20480
	ds_read_b128 v[226:229], v156 offset:22528
	global_load_lds_dwordx4 v128, s[30:31]
	s_add_i32 m0, s59, 0x2000
	s_add_u32 s60, s30, 0x380000
	s_addc_u32 s61, s31, 0
	s_add_i32 s59, s44, s36
	global_load_lds_dwordx4 v130, s[30:31]
	s_mov_b32 m0, s59
	s_add_u32 s62, s30, 0x80
	s_addc_u32 s63, s31, 0
	global_load_lds_dwordx4 v128, s[60:61]
	s_add_i32 m0, s59, 0x2000
	s_add_u32 s64, s34, 0x80
	s_addc_u32 s65, s35, 0
	global_load_lds_dwordx4 v130, s[60:61]
	s_mov_b32 m0, s37
	s_nop 0
	global_load_lds_dwordx4 v128, s[34:35]
	s_mov_b32 m0, s38
	s_nop 0
	global_load_lds_dwordx4 v130, s[34:35]
	s_waitcnt vmcnt(8)
	s_waitcnt lgkmcnt(0)
	s_barrier
	v_mfma_f32_16x16x32_f16 v[60:63], v[166:169], v[198:201], v[60:63]
	v_mfma_f32_16x16x32_f16 v[60:63], v[170:173], v[206:209], v[60:63]
	v_mfma_f32_16x16x32_f16 v[56:59], v[178:181], v[206:209], v[56:59]
	v_mfma_f32_16x16x32_f16 v[56:59], v[174:177], v[198:201], v[56:59]
	v_mfma_f32_16x16x32_f16 v[48:51], v[174:177], v[202:205], v[48:51]
	v_mfma_f32_16x16x32_f16 v[48:51], v[178:181], v[210:213], v[48:51]
	v_mfma_f32_16x16x32_f16 v[52:55], v[170:173], v[210:213], v[52:55]
	v_mfma_f32_16x16x32_f16 v[52:55], v[166:169], v[202:205], v[52:55]
	v_mfma_f32_16x16x32_f16 v[40:43], v[166:169], v[214:217], v[40:43]
	v_mfma_f32_16x16x32_f16 v[40:43], v[170:173], v[222:225], v[40:43]
	v_mfma_f32_16x16x32_f16 v[32:35], v[178:181], v[222:225], v[32:35]
	v_mfma_f32_16x16x32_f16 v[32:35], v[174:177], v[214:217], v[32:35]
	v_mfma_f32_16x16x32_f16 v[8:11], v[174:177], v[218:221], v[8:11]
	v_mfma_f32_16x16x32_f16 v[8:11], v[178:181], v[226:229], v[8:11]
	v_mfma_f32_16x16x32_f16 v[12:15], v[170:173], v[226:229], v[12:15]
	v_mfma_f32_16x16x32_f16 v[12:15], v[166:169], v[218:221], v[12:15]
	v_mfma_f32_16x16x32_f16 v[44:47], v[182:185], v[198:201], v[44:47]
	v_mfma_f32_16x16x32_f16 v[44:47], v[186:189], v[206:209], v[44:47]
	v_mfma_f32_16x16x32_f16 v[36:39], v[194:197], v[206:209], v[36:39]
	v_mfma_f32_16x16x32_f16 v[36:39], v[190:193], v[198:201], v[36:39]
	v_mfma_f32_16x16x32_f16 v[24:27], v[190:193], v[202:205], v[24:27]
	v_mfma_f32_16x16x32_f16 v[24:27], v[194:197], v[210:213], v[24:27]
	v_mfma_f32_16x16x32_f16 v[28:31], v[186:189], v[210:213], v[28:31]
	v_mfma_f32_16x16x32_f16 v[28:31], v[182:185], v[202:205], v[28:31]
	v_mfma_f32_16x16x32_f16 v[20:23], v[182:185], v[214:217], v[20:23]
	v_mfma_f32_16x16x32_f16 v[20:23], v[186:189], v[222:225], v[20:23]
	v_mfma_f32_16x16x32_f16 v[16:19], v[194:197], v[222:225], v[16:19]
	v_mfma_f32_16x16x32_f16 v[16:19], v[190:193], v[214:217], v[16:19]
	v_mfma_f32_16x16x32_f16 v[0:3], v[190:193], v[218:221], v[0:3]
	v_mfma_f32_16x16x32_f16 v[0:3], v[194:197], v[226:229], v[0:3]
	v_mfma_f32_16x16x32_f16 v[4:7], v[186:189], v[226:229], v[4:7]
	v_mfma_f32_16x16x32_f16 v[4:7], v[182:185], v[218:221], v[4:7]
	s_barrier
	s_add_u32 s34, s34, 0x380000
	s_addc_u32 s35, s35, 0
	s_mov_b32 m0, s39
	ds_read_b128 v[166:169], v157
	ds_read_b128 v[170:173], v158
	ds_read_b128 v[174:177], v159
	ds_read_b128 v[178:181], v160
	ds_read_b128 v[182:185], v161
	ds_read_b128 v[186:189], v162
	ds_read_b128 v[190:193], v163
	ds_read_b128 v[194:197], v164
	ds_read_b128 v[198:201], v155 offset:32768
	ds_read_b128 v[202:205], v155 offset:34816
	ds_read_b128 v[206:209], v156 offset:32768
	ds_read_b128 v[210:213], v156 offset:34816
	ds_read_b128 v[214:217], v155 offset:36864
	ds_read_b128 v[218:221], v155 offset:38912
	ds_read_b128 v[222:225], v156 offset:36864
	ds_read_b128 v[226:229], v156 offset:38912
	global_load_lds_dwordx4 v128, s[34:35]
	s_mov_b32 m0, s40
	s_nop 0
	global_load_lds_dwordx4 v130, s[34:35]
	s_waitcnt vmcnt(8)
	s_waitcnt lgkmcnt(0)
	s_barrier
	v_mfma_f32_16x16x32_f16 v[124:127], v[166:169], v[198:201], v[124:127]
	v_mfma_f32_16x16x32_f16 v[124:127], v[170:173], v[206:209], v[124:127]
	v_mfma_f32_16x16x32_f16 v[120:123], v[178:181], v[206:209], v[120:123]
	v_mfma_f32_16x16x32_f16 v[120:123], v[174:177], v[198:201], v[120:123]
	v_mfma_f32_16x16x32_f16 v[112:115], v[174:177], v[202:205], v[112:115]
	v_mfma_f32_16x16x32_f16 v[112:115], v[178:181], v[210:213], v[112:115]
	v_mfma_f32_16x16x32_f16 v[116:119], v[170:173], v[210:213], v[116:119]
	v_mfma_f32_16x16x32_f16 v[116:119], v[166:169], v[202:205], v[116:119]
	v_mfma_f32_16x16x32_f16 v[108:111], v[166:169], v[214:217], v[108:111]
	v_mfma_f32_16x16x32_f16 v[108:111], v[170:173], v[222:225], v[108:111]
	v_mfma_f32_16x16x32_f16 v[100:103], v[178:181], v[222:225], v[100:103]
	v_mfma_f32_16x16x32_f16 v[100:103], v[174:177], v[214:217], v[100:103]
	v_mfma_f32_16x16x32_f16 v[84:87], v[174:177], v[218:221], v[84:87]
	v_mfma_f32_16x16x32_f16 v[84:87], v[178:181], v[226:229], v[84:87]
	v_mfma_f32_16x16x32_f16 v[92:95], v[170:173], v[226:229], v[92:95]
	v_mfma_f32_16x16x32_f16 v[92:95], v[166:169], v[218:221], v[92:95]
	v_mfma_f32_16x16x32_f16 v[104:107], v[182:185], v[198:201], v[104:107]
	v_mfma_f32_16x16x32_f16 v[104:107], v[186:189], v[206:209], v[104:107]
	v_mfma_f32_16x16x32_f16 v[96:99], v[194:197], v[206:209], v[96:99]
	v_mfma_f32_16x16x32_f16 v[96:99], v[190:193], v[198:201], v[96:99]
	v_mfma_f32_16x16x32_f16 v[80:83], v[190:193], v[202:205], v[80:83]
	v_mfma_f32_16x16x32_f16 v[80:83], v[194:197], v[210:213], v[80:83]
	v_mfma_f32_16x16x32_f16 v[88:91], v[186:189], v[210:213], v[88:91]
	v_mfma_f32_16x16x32_f16 v[88:91], v[182:185], v[202:205], v[88:91]
	v_mfma_f32_16x16x32_f16 v[76:79], v[182:185], v[214:217], v[76:79]
	v_mfma_f32_16x16x32_f16 v[76:79], v[186:189], v[222:225], v[76:79]
	v_mfma_f32_16x16x32_f16 v[72:75], v[194:197], v[222:225], v[72:75]
	v_mfma_f32_16x16x32_f16 v[72:75], v[190:193], v[214:217], v[72:75]
	v_mfma_f32_16x16x32_f16 v[64:67], v[190:193], v[218:221], v[64:67]
	v_mfma_f32_16x16x32_f16 v[64:67], v[194:197], v[226:229], v[64:67]
	v_mfma_f32_16x16x32_f16 v[68:71], v[186:189], v[226:229], v[68:71]
	v_mfma_f32_16x16x32_f16 v[68:71], v[182:185], v[218:221], v[68:71]
	s_barrier
	s_add_i32 s34, s46, s36
	s_mov_b32 m0, s34
	ds_read_b128 v[198:201], v155 offset:49152
	ds_read_b128 v[202:205], v155 offset:51200
	ds_read_b128 v[206:209], v156 offset:49152
	ds_read_b128 v[210:213], v156 offset:51200
	ds_read_b128 v[214:217], v155 offset:53248
	ds_read_b128 v[218:221], v155 offset:55296
	ds_read_b128 v[222:225], v156 offset:53248
	ds_read_b128 v[226:229], v156 offset:55296
	global_load_lds_dwordx4 v128, s[62:63]
	s_add_i32 m0, s34, 0x2000
	s_add_u32 s30, s30, 0x380080
	s_addc_u32 s31, s31, 0
	s_add_i32 s34, s47, s36
	global_load_lds_dwordx4 v130, s[62:63]
	s_mov_b32 m0, s34
	s_nop 0
	global_load_lds_dwordx4 v128, s[30:31]
	s_add_i32 m0, s34, 0x2000
	s_nop 0
	global_load_lds_dwordx4 v130, s[30:31]
	s_mov_b32 m0, s41
	s_nop 0
	global_load_lds_dwordx4 v128, s[64:65]
	s_mov_b32 m0, s42
	s_nop 0
	global_load_lds_dwordx4 v130, s[64:65]
	s_waitcnt vmcnt(8)
	s_waitcnt lgkmcnt(0)
	s_barrier
	v_mfma_f32_16x16x32_f16 v[60:63], v[166:169], v[198:201], v[60:63]
	v_mfma_f32_16x16x32_f16 v[60:63], v[170:173], v[206:209], v[60:63]
	v_mfma_f32_16x16x32_f16 v[56:59], v[178:181], v[206:209], v[56:59]
	v_mfma_f32_16x16x32_f16 v[56:59], v[174:177], v[198:201], v[56:59]
	v_mfma_f32_16x16x32_f16 v[48:51], v[174:177], v[202:205], v[48:51]
	v_mfma_f32_16x16x32_f16 v[48:51], v[178:181], v[210:213], v[48:51]
	v_mfma_f32_16x16x32_f16 v[52:55], v[170:173], v[210:213], v[52:55]
	v_mfma_f32_16x16x32_f16 v[52:55], v[166:169], v[202:205], v[52:55]
	v_mfma_f32_16x16x32_f16 v[40:43], v[166:169], v[214:217], v[40:43]
	v_mfma_f32_16x16x32_f16 v[40:43], v[170:173], v[222:225], v[40:43]
	v_mfma_f32_16x16x32_f16 v[32:35], v[178:181], v[222:225], v[32:35]
	v_mfma_f32_16x16x32_f16 v[32:35], v[174:177], v[214:217], v[32:35]
	v_mfma_f32_16x16x32_f16 v[8:11], v[174:177], v[218:221], v[8:11]
	v_mfma_f32_16x16x32_f16 v[8:11], v[178:181], v[226:229], v[8:11]
	v_mfma_f32_16x16x32_f16 v[12:15], v[170:173], v[226:229], v[12:15]
	v_mfma_f32_16x16x32_f16 v[12:15], v[166:169], v[218:221], v[12:15]
	v_mfma_f32_16x16x32_f16 v[44:47], v[182:185], v[198:201], v[44:47]
	v_mfma_f32_16x16x32_f16 v[44:47], v[186:189], v[206:209], v[44:47]
	v_mfma_f32_16x16x32_f16 v[36:39], v[194:197], v[206:209], v[36:39]
	v_mfma_f32_16x16x32_f16 v[36:39], v[190:193], v[198:201], v[36:39]
	v_mfma_f32_16x16x32_f16 v[24:27], v[190:193], v[202:205], v[24:27]
	v_mfma_f32_16x16x32_f16 v[24:27], v[194:197], v[210:213], v[24:27]
	v_mfma_f32_16x16x32_f16 v[28:31], v[186:189], v[210:213], v[28:31]
	v_mfma_f32_16x16x32_f16 v[28:31], v[182:185], v[202:205], v[28:31]
	v_mfma_f32_16x16x32_f16 v[20:23], v[182:185], v[214:217], v[20:23]
	v_mfma_f32_16x16x32_f16 v[20:23], v[186:189], v[222:225], v[20:23]
	v_mfma_f32_16x16x32_f16 v[16:19], v[194:197], v[222:225], v[16:19]
	v_mfma_f32_16x16x32_f16 v[16:19], v[190:193], v[214:217], v[16:19]
	v_mfma_f32_16x16x32_f16 v[0:3], v[190:193], v[218:221], v[0:3]
	v_mfma_f32_16x16x32_f16 v[0:3], v[194:197], v[226:229], v[0:3]
	v_mfma_f32_16x16x32_f16 v[4:7], v[186:189], v[226:229], v[4:7]
	v_mfma_f32_16x16x32_f16 v[4:7], v[182:185], v[218:221], v[4:7]
	s_barrier
	s_add_i32 s58, s58, 2
	s_add_u32 s56, s56, 0x100
	s_addc_u32 s57, s57, 0
	s_add_u32 s28, s28, 0x100
	s_addc_u32 s29, s29, 0
	s_cmpk_gt_u32 s58, 0xdd
	s_cbranch_scc0 .LBB2_20
	v_lshl_add_u32 v144, s55, 8, v137
	v_ashrrev_i32_e32 v145, 31, v144
	v_lshl_add_u64 v[138:139], v[144:145], 2, s[10:11]
	global_load_dword v136, v[138:139], off
	global_load_dword v140, v[138:139], off offset:64
	global_load_dword v142, v[138:139], off offset:128
	global_load_dword v146, v[138:139], off offset:192
	global_load_dword v148, v[138:139], off offset:512
	global_load_dword v174, v[138:139], off offset:576
	global_load_dword v176, v[138:139], off offset:640
	s_nop 0
	global_load_dword v138, v[138:139], off offset:704
	v_lshl_or_b32 v166, s54, 8, v141
	v_ashrrev_i32_e32 v167, 31, v166
	v_or_b32_e32 v168, 16, v144
	v_or_b32_e32 v170, 32, v144
	v_or_b32_e32 v172, 48, v144
	v_lshl_add_u64 v[166:167], v[166:167], 2, s[8:9]
	v_lshlrev_b64 v[144:145], 14, v[144:145]
	v_ashrrev_i32_e32 v169, 31, v168
	v_ashrrev_i32_e32 v171, 31, v170
	v_ashrrev_i32_e32 v173, 31, v172
	v_lshl_add_u64 v[144:145], v[166:167], 0, v[144:145]
	v_lshlrev_b64 v[168:169], 14, v[168:169]
	v_lshlrev_b64 v[170:171], 14, v[170:171]
	v_lshlrev_b64 v[172:173], 14, v[172:173]
	v_add_co_u32_e32 v178, vcc, s48, v144
	v_lshl_add_u64 v[168:169], v[166:167], 0, v[168:169]
	v_lshl_add_u64 v[170:171], v[166:167], 0, v[170:171]
	v_lshl_add_u64 v[166:167], v[166:167], 0, v[172:173]
	v_lshl_add_u64 v[172:173], v[144:145], 0, s[16:17]
	v_addc_co_u32_e32 v179, vcc, 0, v145, vcc
	s_mov_b32 s55, s45
	s_mov_b32 s54, s53
	s_mov_b64 s[28:29], s[26:27]
	s_mov_b64 s[30:31], s[24:25]
	s_waitcnt vmcnt(0)
	v_pk_mul_f32 v[126:127], v[136:137], v[126:127] op_sel_hi:[0,1]
	v_pk_mul_f32 v[124:125], v[136:137], v[124:125] op_sel_hi:[0,1]
	v_pk_mul_f32 v[122:123], v[136:137], v[122:123] op_sel_hi:[0,1]
	v_pk_mul_f32 v[120:121], v[136:137], v[120:121] op_sel_hi:[0,1]
	v_pk_mul_f32 v[46:47], v[148:149], v[46:47] op_sel_hi:[0,1]
	v_pk_mul_f32 v[44:45], v[148:149], v[44:45] op_sel_hi:[0,1]
	v_pk_mul_f32 v[106:107], v[136:137], v[106:107] op_sel_hi:[0,1]
	v_pk_mul_f32 v[104:105], v[136:137], v[104:105] op_sel_hi:[0,1]
	v_pk_mul_f32 v[98:99], v[136:137], v[98:99] op_sel_hi:[0,1]
	v_pk_mul_f32 v[96:97], v[136:137], v[96:97] op_sel_hi:[0,1]
	v_pk_mul_f32 v[118:119], v[140:141], v[118:119] op_sel_hi:[0,1]
	v_pk_mul_f32 v[116:117], v[140:141], v[116:117] op_sel_hi:[0,1]
	v_pk_mul_f32 v[114:115], v[140:141], v[114:115] op_sel_hi:[0,1]
	v_pk_mul_f32 v[112:113], v[140:141], v[112:113] op_sel_hi:[0,1]
	v_pk_mul_f32 v[90:91], v[140:141], v[90:91] op_sel_hi:[0,1]
	v_pk_mul_f32 v[88:89], v[140:141], v[88:89] op_sel_hi:[0,1]
	v_pk_mul_f32 v[82:83], v[140:141], v[82:83] op_sel_hi:[0,1]
	v_pk_mul_f32 v[80:81], v[140:141], v[80:81] op_sel_hi:[0,1]
	v_pk_mul_f32 v[110:111], v[142:143], v[110:111] op_sel_hi:[0,1]
	v_pk_mul_f32 v[108:109], v[142:143], v[108:109] op_sel_hi:[0,1]
	v_pk_mul_f32 v[102:103], v[142:143], v[102:103] op_sel_hi:[0,1]
	v_pk_mul_f32 v[100:101], v[142:143], v[100:101] op_sel_hi:[0,1]
	v_pk_mul_f32 v[78:79], v[142:143], v[78:79] op_sel_hi:[0,1]
	v_pk_mul_f32 v[76:77], v[142:143], v[76:77] op_sel_hi:[0,1]
	v_pk_mul_f32 v[74:75], v[142:143], v[74:75] op_sel_hi:[0,1]
	v_pk_mul_f32 v[72:73], v[142:143], v[72:73] op_sel_hi:[0,1]
	v_pk_mul_f32 v[94:95], v[146:147], v[94:95] op_sel_hi:[0,1]
	v_pk_mul_f32 v[92:93], v[146:147], v[92:93] op_sel_hi:[0,1]
	v_pk_mul_f32 v[86:87], v[146:147], v[86:87] op_sel_hi:[0,1]
	v_pk_mul_f32 v[84:85], v[146:147], v[84:85] op_sel_hi:[0,1]
	v_pk_mul_f32 v[70:71], v[146:147], v[70:71] op_sel_hi:[0,1]
	v_pk_mul_f32 v[68:69], v[146:147], v[68:69] op_sel_hi:[0,1]
	v_pk_mul_f32 v[66:67], v[146:147], v[66:67] op_sel_hi:[0,1]
	v_pk_mul_f32 v[64:65], v[146:147], v[64:65] op_sel_hi:[0,1]
	v_pk_mul_f32 v[62:63], v[148:149], v[62:63] op_sel_hi:[0,1]
	v_pk_mul_f32 v[60:61], v[148:149], v[60:61] op_sel_hi:[0,1]
	global_store_dwordx4 v[144:145], v[124:127], off
	global_store_dwordx4 v[144:145], v[120:123], off offset:64
	global_store_dwordx4 v[144:145], v[104:107], off offset:512
	global_store_dwordx4 v[144:145], v[96:99], off offset:576
	global_store_dwordx4 v[168:169], v[116:119], off
	global_store_dwordx4 v[168:169], v[112:115], off offset:64
	global_store_dwordx4 v[168:169], v[88:91], off offset:512
	global_store_dwordx4 v[168:169], v[80:83], off offset:576
	global_store_dwordx4 v[170:171], v[108:111], off
	global_store_dwordx4 v[170:171], v[100:103], off offset:64
	global_store_dwordx4 v[170:171], v[76:79], off offset:512
	global_store_dwordx4 v[170:171], v[72:75], off offset:576
	global_store_dwordx4 v[166:167], v[92:95], off
	global_store_dwordx4 v[166:167], v[84:87], off offset:64
	global_store_dwordx4 v[166:167], v[68:71], off offset:512
	global_store_dwordx4 v[166:167], v[64:67], off offset:576
	global_store_dwordx4 v[178:179], v[60:63], off
	global_store_dwordx4 v[172:173], v[44:47], off offset:512
	v_pk_mul_f32 v[30:31], v[174:175], v[30:31] op_sel_hi:[0,1]
	v_pk_mul_f32 v[28:29], v[174:175], v[28:29] op_sel_hi:[0,1]
	v_add_co_u32_e32 v46, vcc, s49, v144
	v_lshl_add_u64 v[44:45], v[144:145], 0, s[18:19]
	s_nop 0
	v_addc_co_u32_e32 v47, vcc, 0, v145, vcc
	global_store_dwordx4 v[44:45], v[28:31], off offset:512
	v_pk_mul_f32 v[18:19], v[176:177], v[18:19] op_sel_hi:[0,1]
	v_pk_mul_f32 v[16:17], v[176:177], v[16:17] op_sel_hi:[0,1]
	v_add_co_u32_e32 v30, vcc, s50, v144
	v_lshl_add_u64 v[28:29], v[144:145], 0, s[20:21]
	s_nop 0
	v_addc_co_u32_e32 v31, vcc, 0, v145, vcc
	v_pk_mul_f32 v[38:39], v[148:149], v[38:39] op_sel_hi:[0,1]
	v_pk_mul_f32 v[36:37], v[148:149], v[36:37] op_sel_hi:[0,1]
	v_pk_mul_f32 v[26:27], v[174:175], v[26:27] op_sel_hi:[0,1]
	v_pk_mul_f32 v[24:25], v[174:175], v[24:25] op_sel_hi:[0,1]
	global_store_dwordx4 v[28:29], v[16:19], off offset:576
	global_store_dwordx4 v[172:173], v[36:39], off offset:576
	global_store_dwordx4 v[44:45], v[24:27], off offset:576
	v_add_co_u32_e32 v18, vcc, s51, v144
	v_pk_mul_f32 v[38:39], v[174:175], v[54:55] op_sel_hi:[0,1]
	v_pk_mul_f32 v[36:37], v[174:175], v[52:53] op_sel_hi:[0,1]
	v_pk_mul_f32 v[26:27], v[176:177], v[42:43] op_sel_hi:[0,1]
	v_pk_mul_f32 v[24:25], v[176:177], v[40:41] op_sel_hi:[0,1]
	v_addc_co_u32_e32 v19, vcc, 0, v145, vcc
	v_pk_mul_f32 v[58:59], v[148:149], v[58:59] op_sel_hi:[0,1]
	v_pk_mul_f32 v[56:57], v[148:149], v[56:57] op_sel_hi:[0,1]
	global_store_dwordx4 v[46:47], v[36:39], off
	global_store_dwordx4 v[30:31], v[24:27], off
	v_pk_mul_f32 v[22:23], v[176:177], v[22:23] op_sel_hi:[0,1]
	v_pk_mul_f32 v[38:39], v[174:175], v[50:51] op_sel_hi:[0,1]
	v_pk_mul_f32 v[36:37], v[174:175], v[48:49] op_sel_hi:[0,1]
	v_pk_mul_f32 v[26:27], v[176:177], v[34:35] op_sel_hi:[0,1]
	v_pk_mul_f32 v[24:25], v[176:177], v[32:33] op_sel_hi:[0,1]
	v_pk_mul_f32 v[20:21], v[176:177], v[20:21] op_sel_hi:[0,1]
	v_lshl_add_u64 v[16:17], v[144:145], 0, s[22:23]
	v_pk_mul_f32 v[14:15], v[138:139], v[14:15] op_sel_hi:[0,1]
	v_pk_mul_f32 v[12:13], v[138:139], v[12:13] op_sel_hi:[0,1]
	v_pk_mul_f32 v[10:11], v[138:139], v[10:11] op_sel_hi:[0,1]
	v_pk_mul_f32 v[8:9], v[138:139], v[8:9] op_sel_hi:[0,1]
	v_pk_mul_f32 v[6:7], v[138:139], v[6:7] op_sel_hi:[0,1]
	v_pk_mul_f32 v[4:5], v[138:139], v[4:5] op_sel_hi:[0,1]
	v_pk_mul_f32 v[2:3], v[138:139], v[2:3] op_sel_hi:[0,1]
	v_pk_mul_f32 v[0:1], v[138:139], v[0:1] op_sel_hi:[0,1]
	s_mov_b64 vcc, s[0:1]
	global_store_dwordx4 v[172:173], v[56:59], off offset:64
	global_store_dwordx4 v[44:45], v[36:39], off offset:64
	global_store_dwordx4 v[28:29], v[24:27], off offset:64
	global_store_dwordx4 v[28:29], v[20:23], off offset:512
	global_store_dwordx4 v[18:19], v[12:15], off
	global_store_dwordx4 v[16:17], v[8:11], off offset:64
	global_store_dwordx4 v[16:17], v[4:7], off offset:512
	global_store_dwordx4 v[16:17], v[0:3], off offset:576
	s_cbranch_vccz .LBB2_8
	s_waitcnt vmcnt(0)
	s_cmpk_gt_u32 s33, 0xff
	s_cbranch_scc1 .LBB2_24
	s_barrier
